# P6 router-weight LDS transpose fill: 16 serialized load+wait iterations unrolled with all loads in flight
# baseline (speedup 1.0000x reference)
.LBB0_2119:
	v_lshlrev_b32_e32 v2, 4, v4
	v_and_b32_e32 v5, 3, v4
	v_and_b32_e32 v6, -4, v4
	v_lshl_add_u32 v5, v5, 15, v6
	v_mov_b32_e32 v108, v2
	v_add_u32_e32 v109, 0x2000, v2
	v_add_u32_e32 v110, 0x4000, v2
	v_add_u32_e32 v111, 0x6000, v2
	v_add_u32_e32 v112, 0x8000, v2
	v_add_u32_e32 v113, 0xa000, v2
	v_add_u32_e32 v114, 0xc000, v2
	v_add_u32_e32 v115, 0xe000, v2
	v_add_u32_e32 v116, 0x10000, v2
	v_add_u32_e32 v117, 0x12000, v2
	v_add_u32_e32 v118, 0x14000, v2
	v_add_u32_e32 v119, 0x16000, v2
	v_add_u32_e32 v120, 0x18000, v2
	v_add_u32_e32 v121, 0x1a000, v2
	v_add_u32_e32 v122, 0x1c000, v2
	v_add_u32_e32 v123, 0x1e000, v2
	global_load_dwordx4 v[44:47], v108, s[34:35]
	global_load_dwordx4 v[48:51], v109, s[34:35]
	global_load_dwordx4 v[52:55], v110, s[34:35]
	global_load_dwordx4 v[56:59], v111, s[34:35]
	global_load_dwordx4 v[60:63], v112, s[34:35]
	global_load_dwordx4 v[64:67], v113, s[34:35]
	global_load_dwordx4 v[68:71], v114, s[34:35]
	global_load_dwordx4 v[72:75], v115, s[34:35]
	global_load_dwordx4 v[76:79], v116, s[34:35]
	global_load_dwordx4 v[80:83], v117, s[34:35]
	global_load_dwordx4 v[84:87], v118, s[34:35]
	global_load_dwordx4 v[88:91], v119, s[34:35]
	global_load_dwordx4 v[92:95], v120, s[34:35]
	global_load_dwordx4 v[96:99], v121, s[34:35]
	global_load_dwordx4 v[100:103], v122, s[34:35]
	global_load_dwordx4 v[104:107], v123, s[34:35]
	s_waitcnt vmcnt(15)
	ds_write2st64_b32 v5, v44, v45 offset0:0 offset1:32
	ds_write2st64_b32 v5, v46, v47 offset0:64 offset1:96
	s_waitcnt vmcnt(14)
	ds_write2st64_b32 v5, v48, v49 offset0:2 offset1:34
	ds_write2st64_b32 v5, v50, v51 offset0:66 offset1:98
	s_waitcnt vmcnt(13)
	ds_write2st64_b32 v5, v52, v53 offset0:4 offset1:36
	ds_write2st64_b32 v5, v54, v55 offset0:68 offset1:100
	s_waitcnt vmcnt(12)
	ds_write2st64_b32 v5, v56, v57 offset0:6 offset1:38
	ds_write2st64_b32 v5, v58, v59 offset0:70 offset1:102
	s_waitcnt vmcnt(11)
	ds_write2st64_b32 v5, v60, v61 offset0:8 offset1:40
	ds_write2st64_b32 v5, v62, v63 offset0:72 offset1:104
	s_waitcnt vmcnt(10)
	ds_write2st64_b32 v5, v64, v65 offset0:10 offset1:42
	ds_write2st64_b32 v5, v66, v67 offset0:74 offset1:106
	s_waitcnt vmcnt(9)
	ds_write2st64_b32 v5, v68, v69 offset0:12 offset1:44
	ds_write2st64_b32 v5, v70, v71 offset0:76 offset1:108
	s_waitcnt vmcnt(8)
	ds_write2st64_b32 v5, v72, v73 offset0:14 offset1:46
	ds_write2st64_b32 v5, v74, v75 offset0:78 offset1:110
	s_waitcnt vmcnt(7)
	ds_write2st64_b32 v5, v76, v77 offset0:16 offset1:48
	ds_write2st64_b32 v5, v78, v79 offset0:80 offset1:112
	s_waitcnt vmcnt(6)
	ds_write2st64_b32 v5, v80, v81 offset0:18 offset1:50
	ds_write2st64_b32 v5, v82, v83 offset0:82 offset1:114
	s_waitcnt vmcnt(5)
	ds_write2st64_b32 v5, v84, v85 offset0:20 offset1:52
	ds_write2st64_b32 v5, v86, v87 offset0:84 offset1:116
	s_waitcnt vmcnt(4)
	ds_write2st64_b32 v5, v88, v89 offset0:22 offset1:54
	ds_write2st64_b32 v5, v90, v91 offset0:86 offset1:118
	s_waitcnt vmcnt(3)
	ds_write2st64_b32 v5, v92, v93 offset0:24 offset1:56
	ds_write2st64_b32 v5, v94, v95 offset0:88 offset1:120
	s_waitcnt vmcnt(2)
	ds_write2st64_b32 v5, v96, v97 offset0:26 offset1:58
	ds_write2st64_b32 v5, v98, v99 offset0:90 offset1:122
	s_waitcnt vmcnt(1)
	ds_write2st64_b32 v5, v100, v101 offset0:28 offset1:60
	ds_write2st64_b32 v5, v102, v103 offset0:92 offset1:124
	s_waitcnt vmcnt(0)
	ds_write2st64_b32 v5, v104, v105 offset0:30 offset1:62
	ds_write2st64_b32 v5, v106, v107 offset0:94 offset1:126
